# s_setprio inverted: load/stage segment at priority 1, MFMA segment at priority 0
# speedup vs baseline: 1.0032x; 1.0032x over previous
.LBB2_33:
	s_waitcnt vmcnt(6)
	s_barrier
	s_setprio 0
	v_mfma_i32_16x16x64_i8 v[48:51], v[144:147], v[184:187], v[48:51]
	s_add_i32 s74, s74, 2
	v_mfma_i32_16x16x64_i8 v[40:43], v[148:151], v[184:187], v[40:43]
	s_add_u32 s70, s70, 0x100
	s_addc_u32 s71, s71, 0
	v_mfma_i32_16x16x64_i8 v[32:35], v[144:147], v[172:175], v[32:35]
	s_add_u32 s72, s72, 0x100
	s_addc_u32 s73, s73, 0
	v_mfma_i32_16x16x64_i8 v[24:27], v[148:151], v[172:175], v[24:27]
	s_cmp_gt_u32 s74, 13
	v_mfma_i32_16x16x64_i8 v[16:19], v[144:147], v[168:171], v[16:19]
	v_mfma_i32_16x16x64_i8 v[8:11], v[148:151], v[168:171], v[8:11]
	v_mfma_i32_16x16x64_i8 v[4:7], v[144:147], v[160:163], v[4:7]
	v_mfma_i32_16x16x64_i8 v[0:3], v[148:151], v[160:163], v[0:3]
	v_mfma_i32_16x16x64_i8 v[48:51], v[156:159], v[188:191], v[48:51]
	v_mfma_i32_16x16x64_i8 v[40:43], v[152:155], v[188:191], v[40:43]
	v_mfma_i32_16x16x64_i8 v[32:35], v[156:159], v[176:179], v[32:35]
	v_mfma_i32_16x16x64_i8 v[24:27], v[152:155], v[176:179], v[24:27]
	v_mfma_i32_16x16x64_i8 v[16:19], v[156:159], v[180:183], v[16:19]
	v_mfma_i32_16x16x64_i8 v[8:11], v[152:155], v[180:183], v[8:11]
	v_mfma_i32_16x16x64_i8 v[4:7], v[156:159], v[164:167], v[4:7]
	v_mfma_i32_16x16x64_i8 v[0:3], v[152:155], v[164:167], v[0:3]
	s_setprio 1
	s_barrier
	s_cbranch_scc1 .LBB2_50
.LBB2_34:
	ds_read_b128 v[144:147], v203
	ds_read_b128 v[148:151], v203 offset:2048
	ds_read_b128 v[156:159], v204
	ds_read_b128 v[152:155], v204 offset:2048
	s_cmp_lg_u32 s74, 12
	s_cselect_b64 s[0:1], -1, 0
	s_and_b64 s[4:5], s[0:1], exec
	s_cselect_b32 s75, s73, s68
	s_cselect_b32 s16, s72, s69
	s_mov_b32 m0, s53
	s_and_b32 s5, s71, 0xffff
	s_mov_b32 s4, s70
	ds_read_b128 v[184:187], v205
	ds_read_b128 v[172:175], v205 offset:2048
	ds_read_b128 v[188:191], v206
	ds_read_b128 v[176:179], v206 offset:2048
	ds_read_b128 v[168:171], v205 offset:4096
	ds_read_b128 v[160:163], v205 offset:6144
	ds_read_b128 v[180:183], v206 offset:4096
	ds_read_b128 v[164:167], v206 offset:6144
	buffer_load_dwordx4 v193, s[4:7], 0 offen lds
	s_mov_b32 m0, s54
	s_or_b64 s[36:37], s[28:29], s[0:1]
	buffer_load_dwordx4 v197, s[4:7], 0 offen lds
	s_waitcnt lgkmcnt(8)
	s_barrier
	s_waitcnt lgkmcnt(0)
	s_setprio 0
	v_mfma_i32_16x16x64_i8 v[124:127], v[144:147], v[184:187], v[124:127]
	s_xor_b64 s[34:35], s[36:37], -1
	v_mfma_i32_16x16x64_i8 v[120:123], v[148:151], v[184:187], v[120:123]
	v_mfma_i32_16x16x64_i8 v[108:111], v[144:147], v[172:175], v[108:111]
	v_mfma_i32_16x16x64_i8 v[104:107], v[148:151], v[172:175], v[104:107]
	v_mfma_i32_16x16x64_i8 v[96:99], v[144:147], v[168:171], v[96:99]
	v_mfma_i32_16x16x64_i8 v[88:91], v[148:151], v[168:171], v[88:91]
	v_mfma_i32_16x16x64_i8 v[80:83], v[144:147], v[160:163], v[80:83]
	v_mfma_i32_16x16x64_i8 v[72:75], v[148:151], v[160:163], v[72:75]
	v_mfma_i32_16x16x64_i8 v[124:127], v[156:159], v[188:191], v[124:127]
	v_mfma_i32_16x16x64_i8 v[120:123], v[152:155], v[188:191], v[120:123]
	v_mfma_i32_16x16x64_i8 v[108:111], v[156:159], v[176:179], v[108:111]
	v_mfma_i32_16x16x64_i8 v[104:107], v[152:155], v[176:179], v[104:107]
	v_mfma_i32_16x16x64_i8 v[96:99], v[156:159], v[180:183], v[96:99]
	v_mfma_i32_16x16x64_i8 v[88:91], v[152:155], v[180:183], v[88:91]
	v_mfma_i32_16x16x64_i8 v[80:83], v[156:159], v[164:167], v[80:83]
	v_mfma_i32_16x16x64_i8 v[72:75], v[152:155], v[164:167], v[72:75]
	s_setprio 1
	s_barrier
	ds_read_b128 v[128:131], v207
	ds_read_b128 v[132:135], v207 offset:2048
	ds_read_b128 v[140:143], v208
	ds_read_b128 v[136:139], v208 offset:2048
	s_and_b64 vcc, exec, s[34:35]
	s_cbranch_vccnz .LBB2_36
	s_and_b32 s17, s75, 0xffff
	s_mov_b32 s18, s6
	s_mov_b32 s19, s7
	s_mov_b32 m0, s39
	s_nop 0
	buffer_load_dwordx4 v196, s[16:19], 0 offen lds
	s_mov_b32 m0, s40
	s_nop 0
	buffer_load_dwordx4 v198, s[16:19], 0 offen lds
.LBB2_36:
	s_add_u32 s4, s70, 0xfffc0080
	s_addc_u32 s5, s71, -1
	s_barrier
	s_waitcnt lgkmcnt(0)
	s_setprio 0
	v_mfma_i32_16x16x64_i8 v[116:119], v[128:131], v[184:187], v[116:119]
	s_and_b64 s[0:1], s[0:1], exec
	s_cselect_b32 s17, s5, s66
	s_cselect_b32 s4, s4, s67
	v_mfma_i32_16x16x64_i8 v[112:115], v[132:135], v[184:187], v[112:115]
	v_mfma_i32_16x16x64_i8 v[100:103], v[128:131], v[172:175], v[100:103]
	v_mfma_i32_16x16x64_i8 v[92:95], v[132:135], v[172:175], v[92:95]
	v_mfma_i32_16x16x64_i8 v[84:87], v[128:131], v[168:171], v[84:87]
	v_mfma_i32_16x16x64_i8 v[76:79], v[132:135], v[168:171], v[76:79]
	v_mfma_i32_16x16x64_i8 v[68:71], v[128:131], v[160:163], v[68:71]
	v_mfma_i32_16x16x64_i8 v[64:67], v[132:135], v[160:163], v[64:67]
	v_mfma_i32_16x16x64_i8 v[116:119], v[140:143], v[188:191], v[116:119]
	v_mfma_i32_16x16x64_i8 v[112:115], v[136:139], v[188:191], v[112:115]
	v_mfma_i32_16x16x64_i8 v[100:103], v[140:143], v[176:179], v[100:103]
	v_mfma_i32_16x16x64_i8 v[92:95], v[136:139], v[176:179], v[92:95]
	v_mfma_i32_16x16x64_i8 v[84:87], v[140:143], v[180:183], v[84:87]
	v_mfma_i32_16x16x64_i8 v[76:79], v[136:139], v[180:183], v[76:79]
	v_mfma_i32_16x16x64_i8 v[68:71], v[140:143], v[164:167], v[68:71]
	v_mfma_i32_16x16x64_i8 v[64:67], v[136:139], v[164:167], v[64:67]
	s_setprio 1
	s_barrier
	ds_read_b128 v[184:187], v205 offset:16384
	ds_read_b128 v[172:175], v205 offset:18432
	ds_read_b128 v[188:191], v206 offset:16384
	ds_read_b128 v[176:179], v206 offset:18432
	ds_read_b128 v[168:171], v205 offset:20480
	ds_read_b128 v[160:163], v205 offset:22528
	ds_read_b128 v[180:183], v206 offset:20480
	ds_read_b128 v[164:167], v206 offset:22528
	v_cndmask_b32_e64 v194, 0, 1, s[36:37]
	v_cmp_ne_u32_e64 s[0:1], 1, v194
	s_andn2_b64 vcc, exec, s[36:37]
	s_cbranch_vccnz .LBB2_38
	s_and_b32 s5, s17, 0xffff
	s_mov_b32 m0, s38
	s_nop 0
	buffer_load_dwordx4 v193, s[4:7], 0 offen lds
	s_mov_b32 m0, s41
	s_nop 0
	buffer_load_dwordx4 v197, s[4:7], 0 offen lds
.LBB2_38:
	s_barrier
	s_waitcnt lgkmcnt(0)
	s_setprio 0
	v_mfma_i32_16x16x64_i8 v[60:63], v[144:147], v[184:187], v[60:63]
	v_mfma_i32_16x16x64_i8 v[56:59], v[148:151], v[184:187], v[56:59]
	v_mfma_i32_16x16x64_i8 v[52:55], v[144:147], v[172:175], v[52:55]
	v_mfma_i32_16x16x64_i8 v[44:47], v[148:151], v[172:175], v[44:47]
	v_mfma_i32_16x16x64_i8 v[36:39], v[144:147], v[168:171], v[36:39]
	v_mfma_i32_16x16x64_i8 v[28:31], v[148:151], v[168:171], v[28:31]
	v_mfma_i32_16x16x64_i8 v[20:23], v[144:147], v[160:163], v[20:23]
	v_mfma_i32_16x16x64_i8 v[12:15], v[148:151], v[160:163], v[12:15]
	v_mfma_i32_16x16x64_i8 v[60:63], v[156:159], v[188:191], v[60:63]
	v_mfma_i32_16x16x64_i8 v[56:59], v[152:155], v[188:191], v[56:59]
	v_mfma_i32_16x16x64_i8 v[52:55], v[156:159], v[176:179], v[52:55]
	v_mfma_i32_16x16x64_i8 v[44:47], v[152:155], v[176:179], v[44:47]
	v_mfma_i32_16x16x64_i8 v[36:39], v[156:159], v[180:183], v[36:39]
	v_mfma_i32_16x16x64_i8 v[28:31], v[152:155], v[180:183], v[28:31]
	v_mfma_i32_16x16x64_i8 v[20:23], v[156:159], v[164:167], v[20:23]
	v_mfma_i32_16x16x64_i8 v[12:15], v[152:155], v[164:167], v[12:15]
	s_setprio 1
	s_barrier
	s_mov_b64 s[18:19], -1
	s_and_b64 vcc, exec, s[34:35]
	s_cbranch_vccz .LBB2_40
	s_waitcnt vmcnt(0)
	s_mov_b64 s[18:19], 0

.LBB2_42:
	s_barrier
	s_setprio 0
	v_mfma_i32_16x16x64_i8 v[48:51], v[128:131], v[184:187], v[48:51]
	s_add_i32 s5, 0, 0x18000
	v_add_u32_e32 v210, s5, v199
	v_mfma_i32_16x16x64_i8 v[40:43], v[132:135], v[184:187], v[40:43]
	v_add_u32_e32 v211, s5, v200
	v_mfma_i32_16x16x64_i8 v[32:35], v[128:131], v[172:175], v[32:35]
	v_mfma_i32_16x16x64_i8 v[24:27], v[132:135], v[172:175], v[24:27]
	v_mfma_i32_16x16x64_i8 v[16:19], v[128:131], v[168:171], v[16:19]
	v_mfma_i32_16x16x64_i8 v[8:11], v[132:135], v[168:171], v[8:11]
	v_mfma_i32_16x16x64_i8 v[4:7], v[128:131], v[160:163], v[4:7]
	v_mfma_i32_16x16x64_i8 v[0:3], v[132:135], v[160:163], v[0:3]
	v_mfma_i32_16x16x64_i8 v[48:51], v[140:143], v[188:191], v[48:51]
	v_mfma_i32_16x16x64_i8 v[40:43], v[136:139], v[188:191], v[40:43]
	v_mfma_i32_16x16x64_i8 v[32:35], v[140:143], v[176:179], v[32:35]
	v_mfma_i32_16x16x64_i8 v[24:27], v[136:139], v[176:179], v[24:27]
	v_mfma_i32_16x16x64_i8 v[16:19], v[140:143], v[180:183], v[16:19]
	v_mfma_i32_16x16x64_i8 v[8:11], v[136:139], v[180:183], v[8:11]
	v_mfma_i32_16x16x64_i8 v[4:7], v[140:143], v[164:167], v[4:7]
	v_mfma_i32_16x16x64_i8 v[0:3], v[136:139], v[164:167], v[0:3]
	s_setprio 1
	s_barrier
	ds_read_b128 v[128:131], v210
	ds_read_b128 v[132:135], v210 offset:2048
	ds_read_b128 v[140:143], v211
	ds_read_b128 v[136:139], v211 offset:2048
	ds_read_b128 v[184:187], v205 offset:32768
	ds_read_b128 v[172:175], v205 offset:34816
	ds_read_b128 v[188:191], v206 offset:32768
	ds_read_b128 v[176:179], v206 offset:34816
	ds_read_b128 v[168:171], v205 offset:36864
	ds_read_b128 v[160:163], v205 offset:38912
	ds_read_b128 v[180:183], v206 offset:36864
	ds_read_b128 v[164:167], v206 offset:38912
	s_and_b64 vcc, exec, s[0:1]
	s_cbranch_vccnz .LBB2_44
	s_add_u32 s76, s4, 0x40000
	s_addc_u32 s5, s17, 0
	s_and_b32 s77, s5, 0xffff
	s_mov_b32 s78, s6
	s_mov_b32 s79, s7
	s_mov_b32 m0, s44
	s_nop 0
	buffer_load_dwordx4 v193, s[76:79], 0 offen lds
	s_mov_b32 m0, s45
	s_nop 0
	buffer_load_dwordx4 v197, s[76:79], 0 offen lds
.LBB2_44:
	s_waitcnt lgkmcnt(8)
	s_barrier
	s_waitcnt lgkmcnt(0)
	s_setprio 0
	v_mfma_i32_16x16x64_i8 v[124:127], v[128:131], v[184:187], v[124:127]
	v_mfma_i32_16x16x64_i8 v[120:123], v[132:135], v[184:187], v[120:123]
	v_mfma_i32_16x16x64_i8 v[108:111], v[128:131], v[172:175], v[108:111]
	v_mfma_i32_16x16x64_i8 v[104:107], v[132:135], v[172:175], v[104:107]
	v_mfma_i32_16x16x64_i8 v[96:99], v[128:131], v[168:171], v[96:99]
	v_mfma_i32_16x16x64_i8 v[88:91], v[132:135], v[168:171], v[88:91]
	v_mfma_i32_16x16x64_i8 v[80:83], v[128:131], v[160:163], v[80:83]
	v_mfma_i32_16x16x64_i8 v[72:75], v[132:135], v[160:163], v[72:75]
	v_mfma_i32_16x16x64_i8 v[124:127], v[140:143], v[188:191], v[124:127]
	v_mfma_i32_16x16x64_i8 v[120:123], v[136:139], v[188:191], v[120:123]
	v_mfma_i32_16x16x64_i8 v[108:111], v[140:143], v[176:179], v[108:111]
	v_mfma_i32_16x16x64_i8 v[104:107], v[136:139], v[176:179], v[104:107]
	v_mfma_i32_16x16x64_i8 v[96:99], v[140:143], v[180:183], v[96:99]
	v_mfma_i32_16x16x64_i8 v[88:91], v[136:139], v[180:183], v[88:91]
	v_mfma_i32_16x16x64_i8 v[80:83], v[140:143], v[164:167], v[80:83]
	v_mfma_i32_16x16x64_i8 v[72:75], v[136:139], v[164:167], v[72:75]
	s_setprio 1
	s_barrier
	s_add_i32 s5, 0, 0x1c000
	v_add_u32_e32 v148, s5, v199
	v_add_u32_e32 v152, s5, v200
	ds_read_b128 v[144:147], v148
	ds_read_b128 v[148:151], v148 offset:2048
	ds_read_b128 v[156:159], v152
	ds_read_b128 v[152:155], v152 offset:2048
	s_and_b64 vcc, exec, s[0:1]
	s_cbranch_vccnz .LBB2_46
	s_add_u32 s76, s16, 0x80
	s_addc_u32 s5, s75, 0
	s_and_b32 s77, s5, 0xffff
	s_mov_b32 s78, s6
	s_mov_b32 s79, s7
	s_mov_b32 m0, s47
	s_nop 0
	buffer_load_dwordx4 v196, s[76:79], 0 offen lds
	s_mov_b32 m0, s48
	s_nop 0
	buffer_load_dwordx4 v198, s[76:79], 0 offen lds
.LBB2_46:
	s_barrier
	s_waitcnt lgkmcnt(0)
	s_setprio 0
	v_mfma_i32_16x16x64_i8 v[116:119], v[144:147], v[184:187], v[116:119]
	v_mfma_i32_16x16x64_i8 v[112:115], v[148:151], v[184:187], v[112:115]
	v_mfma_i32_16x16x64_i8 v[100:103], v[144:147], v[172:175], v[100:103]
	v_mfma_i32_16x16x64_i8 v[92:95], v[148:151], v[172:175], v[92:95]
	v_mfma_i32_16x16x64_i8 v[84:87], v[144:147], v[168:171], v[84:87]
	v_mfma_i32_16x16x64_i8 v[76:79], v[148:151], v[168:171], v[76:79]
	v_mfma_i32_16x16x64_i8 v[68:71], v[144:147], v[160:163], v[68:71]
	v_mfma_i32_16x16x64_i8 v[64:67], v[148:151], v[160:163], v[64:67]
	v_mfma_i32_16x16x64_i8 v[116:119], v[156:159], v[188:191], v[116:119]
	v_mfma_i32_16x16x64_i8 v[112:115], v[152:155], v[188:191], v[112:115]
	v_mfma_i32_16x16x64_i8 v[100:103], v[156:159], v[176:179], v[100:103]
	v_mfma_i32_16x16x64_i8 v[92:95], v[152:155], v[176:179], v[92:95]
	v_mfma_i32_16x16x64_i8 v[84:87], v[156:159], v[180:183], v[84:87]
	v_mfma_i32_16x16x64_i8 v[76:79], v[152:155], v[180:183], v[76:79]
	v_mfma_i32_16x16x64_i8 v[68:71], v[156:159], v[164:167], v[68:71]
	v_mfma_i32_16x16x64_i8 v[64:67], v[152:155], v[164:167], v[64:67]
	s_setprio 1
	s_barrier
	ds_read_b128 v[184:187], v205 offset:49152
	ds_read_b128 v[172:175], v205 offset:51200
	ds_read_b128 v[188:191], v206 offset:49152
	ds_read_b128 v[176:179], v206 offset:51200
	ds_read_b128 v[168:171], v205 offset:53248
	ds_read_b128 v[160:163], v205 offset:55296
	ds_read_b128 v[180:183], v206 offset:53248
	ds_read_b128 v[164:167], v206 offset:55296
	s_and_b64 vcc, exec, s[0:1]
	s_cbranch_vccnz .LBB2_48
	s_add_u32 s4, s4, 0x80
	s_addc_u32 s5, s17, 0
	s_and_b32 s5, s5, 0xffff
	s_mov_b32 m0, s49
	s_nop 0
	buffer_load_dwordx4 v193, s[4:7], 0 offen lds
	s_mov_b32 m0, s50
	s_nop 0
	buffer_load_dwordx4 v197, s[4:7], 0 offen lds
.LBB2_48:
	s_barrier
	s_waitcnt lgkmcnt(0)
	s_setprio 0
	v_mfma_i32_16x16x64_i8 v[60:63], v[128:131], v[184:187], v[60:63]
	v_mfma_i32_16x16x64_i8 v[56:59], v[132:135], v[184:187], v[56:59]
	v_mfma_i32_16x16x64_i8 v[52:55], v[128:131], v[172:175], v[52:55]
	v_mfma_i32_16x16x64_i8 v[44:47], v[132:135], v[172:175], v[44:47]
	v_mfma_i32_16x16x64_i8 v[36:39], v[128:131], v[168:171], v[36:39]
	v_mfma_i32_16x16x64_i8 v[28:31], v[132:135], v[168:171], v[28:31]
	v_mfma_i32_16x16x64_i8 v[20:23], v[128:131], v[160:163], v[20:23]
	v_mfma_i32_16x16x64_i8 v[12:15], v[132:135], v[160:163], v[12:15]
	v_mfma_i32_16x16x64_i8 v[60:63], v[140:143], v[188:191], v[60:63]
	v_mfma_i32_16x16x64_i8 v[56:59], v[136:139], v[188:191], v[56:59]
	v_mfma_i32_16x16x64_i8 v[52:55], v[140:143], v[176:179], v[52:55]
	v_mfma_i32_16x16x64_i8 v[44:47], v[136:139], v[176:179], v[44:47]
	v_mfma_i32_16x16x64_i8 v[36:39], v[140:143], v[180:183], v[36:39]
	v_mfma_i32_16x16x64_i8 v[28:31], v[136:139], v[180:183], v[28:31]
	v_mfma_i32_16x16x64_i8 v[20:23], v[140:143], v[164:167], v[20:23]
	v_mfma_i32_16x16x64_i8 v[12:15], v[136:139], v[164:167], v[12:15]
	s_setprio 1
	s_barrier
	s_and_b64 vcc, exec, s[0:1]
	s_cbranch_vccnz .LBB2_33
	s_add_u32 s4, s16, 0x4080
	s_addc_u32 s0, s75, 0
	s_and_b32 s5, s0, 0xffff
	s_mov_b32 m0, s51
	s_nop 0
	buffer_load_dwordx4 v196, s[4:7], 0 offen lds
	s_mov_b32 m0, s52
	s_nop 0
	buffer_load_dwordx4 v198, s[4:7], 0 offen lds
	s_branch .LBB2_33

.LBB3_3:
	s_waitcnt vmcnt(10)
	s_barrier
	s_setprio 0
	v_mfma_f32_16x16x128_f8f6f4 v[118:121], v[26:33], v[58:65], v[118:121]
	s_add_i32 s50, s50, 2
	s_add_u32 s10, s10, 0x100
	s_addc_u32 s11, s11, 0
	v_mfma_f32_16x16x128_f8f6f4 v[114:117], v[18:25], v[58:65], v[114:117]
	s_cmpk_eq_i32 s10, 0x700
	s_cselect_b64 s[18:19], -1, 0
	s_cmpk_lg_i32 s10, 0x700
	s_cselect_b64 s[26:27], -1, 0
	v_mfma_f32_16x16x128_f8f6f4 v[102:105], v[26:33], v[50:57], v[102:105]
	s_add_u32 s54, s48, s10
	s_addc_u32 s55, s49, s11
	s_add_u32 s51, s8, s10
	s_addc_u32 s52, s25, s11
	v_mfma_f32_16x16x128_f8f6f4 v[98:101], v[18:25], v[50:57], v[98:101]
	s_add_u32 s20, s51, 0x100
	s_addc_u32 s53, s52, 0
	s_add_u32 s12, s54, 0x100080
	s_addc_u32 s0, s55, 0
	v_mfma_f32_16x16x128_f8f6f4 v[86:89], v[26:33], v[42:49], v[86:89]
	s_and_b32 s13, s0, 0xffff
	s_cmp_gt_u32 s50, 13
	v_mfma_f32_16x16x128_f8f6f4 v[82:85], v[18:25], v[42:49], v[82:85]
	v_mfma_f32_16x16x128_f8f6f4 v[70:73], v[26:33], v[34:41], v[70:73]
	v_mfma_f32_16x16x128_f8f6f4 v[66:69], v[18:25], v[34:41], v[66:69]
	s_setprio 1
	s_barrier
	s_cbranch_scc1 .LBB3_20
.LBB3_4:
	ds_read_b128 v[2:5], v203
	ds_read_b128 v[10:13], v203 offset:2048
	ds_read_b128 v[6:9], v204
	ds_read_b128 v[14:17], v204 offset:2048
	s_mov_b32 m0, s46
	ds_read_b128 v[58:61], v200
	ds_read_b128 v[50:53], v200 offset:2048
	ds_read_b128 v[62:65], v201
	ds_read_b128 v[54:57], v201 offset:2048
	ds_read_b128 v[42:45], v200 offset:4096
	ds_read_b128 v[34:37], v200 offset:6144
	ds_read_b128 v[46:49], v201 offset:4096
	ds_read_b128 v[38:41], v201 offset:6144
	s_waitcnt vmcnt(8)
	buffer_load_dwordx4 v1, s[12:15], 0 offen lds
	s_mov_b32 m0, s47
	s_nop 0
	buffer_load_dwordx4 v195, s[12:15], 0 offen lds
	s_waitcnt lgkmcnt(8)
	s_barrier
	s_waitcnt lgkmcnt(0)
	s_setprio 0
	v_mfma_f32_16x16x128_f8f6f4 v[190:193], v[2:9], v[58:65], v[190:193]
	v_mfma_f32_16x16x128_f8f6f4 v[186:189], v[10:17], v[58:65], v[186:189]
	v_mfma_f32_16x16x128_f8f6f4 v[174:177], v[2:9], v[50:57], v[174:177]
	v_mfma_f32_16x16x128_f8f6f4 v[170:173], v[10:17], v[50:57], v[170:173]
	v_mfma_f32_16x16x128_f8f6f4 v[158:161], v[2:9], v[42:49], v[158:161]
	v_mfma_f32_16x16x128_f8f6f4 v[154:157], v[10:17], v[42:49], v[154:157]
	v_mfma_f32_16x16x128_f8f6f4 v[142:145], v[2:9], v[34:41], v[142:145]
	v_mfma_f32_16x16x128_f8f6f4 v[138:141], v[10:17], v[34:41], v[138:141]
	s_setprio 1
	s_barrier
	ds_read_b128 v[26:29], v205
	ds_read_b128 v[18:21], v205 offset:2048
	ds_read_b128 v[30:33], v206
	ds_read_b128 v[22:25], v206 offset:2048
	s_waitcnt vmcnt(8)
	s_and_b64 vcc, exec, s[18:19]
	s_cbranch_vccnz .LBB3_6
	s_and_b32 s21, s53, 0xffff
	s_mov_b32 s22, s14
	s_mov_b32 s23, s15
	s_mov_b32 m0, s33
	s_nop 0
	buffer_load_dwordx4 v194, s[20:23], 0 offen lds
	s_mov_b32 m0, s34
	s_nop 0
	buffer_load_dwordx4 v196, s[20:23], 0 offen lds
.LBB3_6:
	s_barrier
	s_waitcnt lgkmcnt(0)
	s_setprio 0
	v_mfma_f32_16x16x128_f8f6f4 v[182:185], v[26:33], v[58:65], v[182:185]
	s_add_u32 s12, s54, 0x100
	s_addc_u32 s21, s55, 0
	v_mfma_f32_16x16x128_f8f6f4 v[178:181], v[18:25], v[58:65], v[178:181]
	v_mfma_f32_16x16x128_f8f6f4 v[166:169], v[26:33], v[50:57], v[166:169]
	v_mfma_f32_16x16x128_f8f6f4 v[162:165], v[18:25], v[50:57], v[162:165]
	v_mfma_f32_16x16x128_f8f6f4 v[150:153], v[26:33], v[42:49], v[150:153]
	v_mfma_f32_16x16x128_f8f6f4 v[146:149], v[18:25], v[42:49], v[146:149]
	v_mfma_f32_16x16x128_f8f6f4 v[134:137], v[26:33], v[34:41], v[134:137]
	v_mfma_f32_16x16x128_f8f6f4 v[130:133], v[18:25], v[34:41], v[130:133]
	s_setprio 1
	s_barrier
	ds_read_b128 v[58:61], v200 offset:16384
	ds_read_b128 v[50:53], v200 offset:18432
	ds_read_b128 v[62:65], v201 offset:16384
	ds_read_b128 v[54:57], v201 offset:18432
	ds_read_b128 v[42:45], v200 offset:20480
	ds_read_b128 v[34:37], v200 offset:22528
	ds_read_b128 v[46:49], v201 offset:20480
	ds_read_b128 v[38:41], v201 offset:22528
	v_cndmask_b32_e64 v207, 0, 1, s[26:27]
	v_cmp_ne_u32_e64 s[0:1], 1, v207
	s_andn2_b64 vcc, exec, s[26:27]
	s_cbranch_vccnz .LBB3_8
	s_and_b32 s13, s21, 0xffff
	s_mov_b32 m0, s31
	s_nop 0
	buffer_load_dwordx4 v1, s[12:15], 0 offen lds
	s_mov_b32 m0, s35
	s_nop 0
	buffer_load_dwordx4 v195, s[12:15], 0 offen lds
.LBB3_8:
	s_barrier
	s_waitcnt lgkmcnt(0)
	s_setprio 0
	v_mfma_f32_16x16x128_f8f6f4 v[126:129], v[2:9], v[58:65], v[126:129]
	v_mfma_f32_16x16x128_f8f6f4 v[122:125], v[10:17], v[58:65], v[122:125]
	v_mfma_f32_16x16x128_f8f6f4 v[110:113], v[2:9], v[50:57], v[110:113]
	v_mfma_f32_16x16x128_f8f6f4 v[106:109], v[10:17], v[50:57], v[106:109]
	v_mfma_f32_16x16x128_f8f6f4 v[94:97], v[2:9], v[42:49], v[94:97]
	v_mfma_f32_16x16x128_f8f6f4 v[90:93], v[10:17], v[42:49], v[90:93]
	v_mfma_f32_16x16x128_f8f6f4 v[78:81], v[2:9], v[34:41], v[78:81]
	v_mfma_f32_16x16x128_f8f6f4 v[74:77], v[10:17], v[34:41], v[74:77]
	s_setprio 1
	s_barrier
	s_and_b64 vcc, exec, s[0:1]
	s_mov_b64 s[22:23], -1
	s_cbranch_vccnz .LBB3_10
	s_add_u32 s56, s51, 0x10100
	s_addc_u32 s13, s52, 0
	s_mov_b32 m0, s17
	s_and_b32 s57, s13, 0xffff
	s_mov_b32 s58, s14
	s_mov_b32 s59, s15
	buffer_load_dwordx4 v194, s[56:59], 0 offen lds
	s_mov_b32 m0, s36
	s_mov_b64 s[22:23], 0
	buffer_load_dwordx4 v196, s[56:59], 0 offen lds
	s_waitcnt vmcnt(10)

.LBB3_12:
	s_barrier
	s_setprio 0
	v_mfma_f32_16x16x128_f8f6f4 v[118:121], v[26:33], v[58:65], v[118:121]
	s_add_i32 s13, 0, 0x18000
	v_add_u32_e32 v2, s13, v198
	v_add_u32_e32 v6, s13, v199
	v_mfma_f32_16x16x128_f8f6f4 v[114:117], v[18:25], v[58:65], v[114:117]
	v_mfma_f32_16x16x128_f8f6f4 v[102:105], v[26:33], v[50:57], v[102:105]
	v_mfma_f32_16x16x128_f8f6f4 v[98:101], v[18:25], v[50:57], v[98:101]
	v_mfma_f32_16x16x128_f8f6f4 v[86:89], v[26:33], v[42:49], v[86:89]
	v_mfma_f32_16x16x128_f8f6f4 v[82:85], v[18:25], v[42:49], v[82:85]
	v_mfma_f32_16x16x128_f8f6f4 v[70:73], v[26:33], v[34:41], v[70:73]
	v_mfma_f32_16x16x128_f8f6f4 v[66:69], v[18:25], v[34:41], v[66:69]
	s_setprio 1
	s_barrier
	ds_read_b128 v[10:13], v2
	ds_read_b128 v[2:5], v2 offset:2048
	ds_read_b128 v[14:17], v6
	ds_read_b128 v[6:9], v6 offset:2048
	ds_read_b128 v[58:61], v200 offset:32768
	ds_read_b128 v[50:53], v200 offset:34816
	ds_read_b128 v[62:65], v201 offset:32768
	ds_read_b128 v[54:57], v201 offset:34816
	ds_read_b128 v[42:45], v200 offset:36864
	ds_read_b128 v[34:37], v200 offset:38912
	ds_read_b128 v[46:49], v201 offset:36864
	ds_read_b128 v[38:41], v201 offset:38912
	s_waitcnt vmcnt(8)
	s_and_b64 vcc, exec, s[0:1]
	s_cbranch_vccnz .LBB3_14
	s_add_u32 s56, s54, 0x100100
	s_addc_u32 s13, s55, 0
	s_and_b32 s57, s13, 0xffff
	s_mov_b32 s58, s14
	s_mov_b32 s59, s15
	s_mov_b32 m0, s37
	s_nop 0
	buffer_load_dwordx4 v1, s[56:59], 0 offen lds
	s_mov_b32 m0, s38
	s_nop 0
	buffer_load_dwordx4 v195, s[56:59], 0 offen lds
.LBB3_14:
	s_waitcnt lgkmcnt(8)
	s_barrier
	s_waitcnt lgkmcnt(0)
	s_setprio 0
	v_mfma_f32_16x16x128_f8f6f4 v[190:193], v[10:17], v[58:65], v[190:193]
	v_mfma_f32_16x16x128_f8f6f4 v[186:189], v[2:9], v[58:65], v[186:189]
	v_mfma_f32_16x16x128_f8f6f4 v[174:177], v[10:17], v[50:57], v[174:177]
	v_mfma_f32_16x16x128_f8f6f4 v[170:173], v[2:9], v[50:57], v[170:173]
	v_mfma_f32_16x16x128_f8f6f4 v[158:161], v[10:17], v[42:49], v[158:161]
	v_mfma_f32_16x16x128_f8f6f4 v[154:157], v[2:9], v[42:49], v[154:157]
	v_mfma_f32_16x16x128_f8f6f4 v[142:145], v[10:17], v[34:41], v[142:145]
	v_mfma_f32_16x16x128_f8f6f4 v[138:141], v[2:9], v[34:41], v[138:141]
	s_setprio 1
	s_barrier
	s_add_i32 s13, 0, 0x1c000
	v_add_u32_e32 v18, s13, v198
	v_add_u32_e32 v22, s13, v199
	ds_read_b128 v[26:29], v18
	ds_read_b128 v[18:21], v18 offset:2048
	ds_read_b128 v[30:33], v22
	ds_read_b128 v[22:25], v22 offset:2048
	s_waitcnt vmcnt(8)
	s_and_b64 vcc, exec, s[0:1]
	s_cbranch_vccnz .LBB3_16
	s_and_b64 s[22:23], exec, s[18:19]
	s_cselect_b32 s20, s8, s20
	s_cselect_b32 s13, s25, s53
	s_add_u32 s56, s20, 0x80
	s_addc_u32 s13, s13, 0
	s_and_b32 s57, s13, 0xffff
	s_mov_b32 s58, s14
	s_mov_b32 s59, s15
	s_mov_b32 m0, s40
	s_nop 0
	buffer_load_dwordx4 v194, s[56:59], 0 offen lds
	s_mov_b32 m0, s41
	s_nop 0
	buffer_load_dwordx4 v196, s[56:59], 0 offen lds
.LBB3_16:
	s_barrier
	s_waitcnt lgkmcnt(0)
	s_setprio 0
	v_mfma_f32_16x16x128_f8f6f4 v[182:185], v[26:33], v[58:65], v[182:185]
	v_mfma_f32_16x16x128_f8f6f4 v[178:181], v[18:25], v[58:65], v[178:181]
	v_mfma_f32_16x16x128_f8f6f4 v[166:169], v[26:33], v[50:57], v[166:169]
	v_mfma_f32_16x16x128_f8f6f4 v[162:165], v[18:25], v[50:57], v[162:165]
	v_mfma_f32_16x16x128_f8f6f4 v[150:153], v[26:33], v[42:49], v[150:153]
	v_mfma_f32_16x16x128_f8f6f4 v[146:149], v[18:25], v[42:49], v[146:149]
	v_mfma_f32_16x16x128_f8f6f4 v[134:137], v[26:33], v[34:41], v[134:137]
	v_mfma_f32_16x16x128_f8f6f4 v[130:133], v[18:25], v[34:41], v[130:133]
	s_setprio 1
	s_barrier
	ds_read_b128 v[58:61], v200 offset:49152
	ds_read_b128 v[50:53], v200 offset:51200
	ds_read_b128 v[62:65], v201 offset:49152
	ds_read_b128 v[54:57], v201 offset:51200
	ds_read_b128 v[42:45], v200 offset:53248
	ds_read_b128 v[34:37], v200 offset:55296
	ds_read_b128 v[46:49], v201 offset:53248
	ds_read_b128 v[38:41], v201 offset:55296
	s_and_b64 vcc, exec, s[0:1]
	s_cbranch_vccnz .LBB3_18
	s_and_b64 s[18:19], exec, s[18:19]
	s_cselect_b32 s12, s16, s12
	s_cselect_b32 s13, s9, s21
	s_add_u32 s12, s12, 0x80
	s_addc_u32 s13, s13, 0
	s_and_b32 s13, s13, 0xffff
	s_mov_b32 m0, s42
	s_nop 0
	buffer_load_dwordx4 v1, s[12:15], 0 offen lds
	s_mov_b32 m0, s43
	s_nop 0
	buffer_load_dwordx4 v195, s[12:15], 0 offen lds
.LBB3_18:
	s_barrier
	s_waitcnt lgkmcnt(0)
	s_setprio 0
	v_mfma_f32_16x16x128_f8f6f4 v[126:129], v[10:17], v[58:65], v[126:129]
	v_mfma_f32_16x16x128_f8f6f4 v[122:125], v[2:9], v[58:65], v[122:125]
	v_mfma_f32_16x16x128_f8f6f4 v[110:113], v[10:17], v[50:57], v[110:113]
	v_mfma_f32_16x16x128_f8f6f4 v[106:109], v[2:9], v[50:57], v[106:109]
	v_mfma_f32_16x16x128_f8f6f4 v[94:97], v[10:17], v[42:49], v[94:97]
	v_mfma_f32_16x16x128_f8f6f4 v[90:93], v[2:9], v[42:49], v[90:93]
	v_mfma_f32_16x16x128_f8f6f4 v[78:81], v[10:17], v[34:41], v[78:81]
	v_mfma_f32_16x16x128_f8f6f4 v[74:77], v[2:9], v[34:41], v[74:77]
	s_setprio 1
	s_barrier
	s_and_b64 vcc, exec, s[0:1]
	s_cbranch_vccnz .LBB3_3
	s_add_u32 s12, s51, 0x10180
	s_addc_u32 s0, s52, 0
	s_and_b32 s13, s0, 0xffff
	s_mov_b32 m0, s44
	s_nop 0
	buffer_load_dwordx4 v194, s[12:15], 0 offen lds
	s_mov_b32 m0, s45
	s_nop 0
	buffer_load_dwordx4 v196, s[12:15], 0 offen lds
	s_branch .LBB3_3

.LBB4_13:
	s_waitcnt vmcnt(10)
	s_barrier
	s_setprio 0
	v_mfma_f32_16x16x128_f8f6f4 v[116:119], v[24:31], v[56:63], v[116:119]
	s_add_i32 s44, s44, 2
	s_add_u32 s10, s10, 0x100
	s_addc_u32 s11, s11, 0
	v_mfma_f32_16x16x128_f8f6f4 v[112:115], v[16:23], v[56:63], v[112:115]
	s_cmpk_eq_i32 s10, 0x700
	s_cselect_b64 s[18:19], -1, 0
	s_cmpk_lg_i32 s10, 0x700
	s_cselect_b64 s[24:25], -1, 0
	v_mfma_f32_16x16x128_f8f6f4 v[100:103], v[24:31], v[48:55], v[100:103]
	s_add_u32 s49, s16, s10
	s_addc_u32 s50, s9, s11
	s_add_u32 s46, s8, s10
	s_addc_u32 s47, s3, s11
	v_mfma_f32_16x16x128_f8f6f4 v[96:99], v[16:23], v[48:55], v[96:99]
	s_add_u32 s20, s46, 0x100
	s_addc_u32 s48, s47, 0
	s_add_u32 s12, s49, 0x40080
	s_addc_u32 s0, s50, 0
	v_mfma_f32_16x16x128_f8f6f4 v[84:87], v[24:31], v[40:47], v[84:87]
	s_and_b32 s13, s0, 0xffff
	s_cmp_gt_u32 s44, 13
	v_mfma_f32_16x16x128_f8f6f4 v[80:83], v[16:23], v[40:47], v[80:83]
	v_mfma_f32_16x16x128_f8f6f4 v[68:71], v[24:31], v[32:39], v[68:71]
	v_mfma_f32_16x16x128_f8f6f4 v[64:67], v[16:23], v[32:39], v[64:67]
	s_setprio 1
	s_barrier
	s_cbranch_scc1 .LBB4_30
.LBB4_14:
	ds_read_b128 v[0:3], v202
	ds_read_b128 v[8:11], v202 offset:2048
	ds_read_b128 v[4:7], v203
	ds_read_b128 v[12:15], v203 offset:2048
	s_mov_b32 m0, s42
	ds_read_b128 v[56:59], v200
	ds_read_b128 v[48:51], v200 offset:2048
	ds_read_b128 v[60:63], v201
	ds_read_b128 v[52:55], v201 offset:2048
	ds_read_b128 v[40:43], v200 offset:4096
	ds_read_b128 v[32:35], v200 offset:6144
	ds_read_b128 v[44:47], v201 offset:4096
	ds_read_b128 v[36:39], v201 offset:6144
	s_waitcnt vmcnt(8)
	buffer_load_dwordx4 v192, s[12:15], 0 offen lds
	s_mov_b32 m0, s43
	s_nop 0
	buffer_load_dwordx4 v194, s[12:15], 0 offen lds
	s_waitcnt lgkmcnt(8)
	s_barrier
	s_waitcnt lgkmcnt(0)
	s_setprio 0
	v_mfma_f32_16x16x128_f8f6f4 v[188:191], v[0:7], v[56:63], v[188:191]
	v_mfma_f32_16x16x128_f8f6f4 v[184:187], v[8:15], v[56:63], v[184:187]
	v_mfma_f32_16x16x128_f8f6f4 v[172:175], v[0:7], v[48:55], v[172:175]
	v_mfma_f32_16x16x128_f8f6f4 v[168:171], v[8:15], v[48:55], v[168:171]
	v_mfma_f32_16x16x128_f8f6f4 v[156:159], v[0:7], v[40:47], v[156:159]
	v_mfma_f32_16x16x128_f8f6f4 v[152:155], v[8:15], v[40:47], v[152:155]
	v_mfma_f32_16x16x128_f8f6f4 v[140:143], v[0:7], v[32:39], v[140:143]
	v_mfma_f32_16x16x128_f8f6f4 v[136:139], v[8:15], v[32:39], v[136:139]
	s_setprio 1
	s_barrier
	ds_read_b128 v[24:27], v204
	ds_read_b128 v[16:19], v204 offset:2048
	ds_read_b128 v[28:31], v205
	ds_read_b128 v[20:23], v205 offset:2048
	s_waitcnt vmcnt(8)
	s_and_b64 vcc, exec, s[18:19]
	s_cbranch_vccnz .LBB4_16
	s_and_b32 s21, s48, 0xffff
	s_mov_b32 s22, s14
	s_mov_b32 s23, s15
	s_mov_b32 m0, s28
	s_nop 0
	buffer_load_dwordx4 v193, s[20:23], 0 offen lds
	s_mov_b32 m0, s29
	s_nop 0
	buffer_load_dwordx4 v195, s[20:23], 0 offen lds
.LBB4_16:
	s_barrier
	s_waitcnt lgkmcnt(0)
	s_setprio 0
	v_mfma_f32_16x16x128_f8f6f4 v[180:183], v[24:31], v[56:63], v[180:183]
	s_add_u32 s12, s49, 0x100
	s_addc_u32 s21, s50, 0
	v_mfma_f32_16x16x128_f8f6f4 v[176:179], v[16:23], v[56:63], v[176:179]
	v_mfma_f32_16x16x128_f8f6f4 v[164:167], v[24:31], v[48:55], v[164:167]
	v_mfma_f32_16x16x128_f8f6f4 v[160:163], v[16:23], v[48:55], v[160:163]
	v_mfma_f32_16x16x128_f8f6f4 v[148:151], v[24:31], v[40:47], v[148:151]
	v_mfma_f32_16x16x128_f8f6f4 v[144:147], v[16:23], v[40:47], v[144:147]
	v_mfma_f32_16x16x128_f8f6f4 v[132:135], v[24:31], v[32:39], v[132:135]
	v_mfma_f32_16x16x128_f8f6f4 v[128:131], v[16:23], v[32:39], v[128:131]
	s_setprio 1
	s_barrier
	ds_read_b128 v[56:59], v200 offset:16384
	ds_read_b128 v[48:51], v200 offset:18432
	ds_read_b128 v[60:63], v201 offset:16384
	ds_read_b128 v[52:55], v201 offset:18432
	ds_read_b128 v[40:43], v200 offset:20480
	ds_read_b128 v[32:35], v200 offset:22528
	ds_read_b128 v[44:47], v201 offset:20480
	ds_read_b128 v[36:39], v201 offset:22528
	v_cndmask_b32_e64 v206, 0, 1, s[24:25]
	v_cmp_ne_u32_e64 s[0:1], 1, v206
	s_andn2_b64 vcc, exec, s[24:25]
	s_cbranch_vccnz .LBB4_18
	s_and_b32 s13, s21, 0xffff
	s_mov_b32 m0, s7
	s_nop 0
	buffer_load_dwordx4 v192, s[12:15], 0 offen lds
	s_mov_b32 m0, s30
	s_nop 0
	buffer_load_dwordx4 v194, s[12:15], 0 offen lds
.LBB4_18:
	s_barrier
	s_waitcnt lgkmcnt(0)
	s_setprio 0
	v_mfma_f32_16x16x128_f8f6f4 v[124:127], v[0:7], v[56:63], v[124:127]
	v_mfma_f32_16x16x128_f8f6f4 v[120:123], v[8:15], v[56:63], v[120:123]
	v_mfma_f32_16x16x128_f8f6f4 v[108:111], v[0:7], v[48:55], v[108:111]
	v_mfma_f32_16x16x128_f8f6f4 v[104:107], v[8:15], v[48:55], v[104:107]
	v_mfma_f32_16x16x128_f8f6f4 v[92:95], v[0:7], v[40:47], v[92:95]
	v_mfma_f32_16x16x128_f8f6f4 v[88:91], v[8:15], v[40:47], v[88:91]
	v_mfma_f32_16x16x128_f8f6f4 v[76:79], v[0:7], v[32:39], v[76:79]
	v_mfma_f32_16x16x128_f8f6f4 v[72:75], v[8:15], v[32:39], v[72:75]
	s_setprio 1
	s_barrier
	s_and_b64 vcc, exec, s[0:1]
	s_mov_b64 s[22:23], -1
	s_cbranch_vccnz .LBB4_20
	s_add_u32 s52, s46, 0x4100
	s_addc_u32 s13, s47, 0
	s_mov_b32 m0, s17
	s_and_b32 s53, s13, 0xffff
	s_mov_b32 s54, s14
	s_mov_b32 s55, s15
	buffer_load_dwordx4 v193, s[52:55], 0 offen lds
	s_mov_b32 m0, s31
	s_mov_b64 s[22:23], 0
	buffer_load_dwordx4 v195, s[52:55], 0 offen lds
	s_waitcnt vmcnt(10)

.LBB4_22:
	s_barrier
	s_setprio 0
	v_mfma_f32_16x16x128_f8f6f4 v[116:119], v[24:31], v[56:63], v[116:119]
	v_add_u32_e32 v0, s45, v198
	v_add_u32_e32 v4, s45, v199
	v_mfma_f32_16x16x128_f8f6f4 v[112:115], v[16:23], v[56:63], v[112:115]
	v_mfma_f32_16x16x128_f8f6f4 v[100:103], v[24:31], v[48:55], v[100:103]
	v_mfma_f32_16x16x128_f8f6f4 v[96:99], v[16:23], v[48:55], v[96:99]
	v_mfma_f32_16x16x128_f8f6f4 v[84:87], v[24:31], v[40:47], v[84:87]
	v_mfma_f32_16x16x128_f8f6f4 v[80:83], v[16:23], v[40:47], v[80:83]
	v_mfma_f32_16x16x128_f8f6f4 v[68:71], v[24:31], v[32:39], v[68:71]
	v_mfma_f32_16x16x128_f8f6f4 v[64:67], v[16:23], v[32:39], v[64:67]
	s_setprio 1
	s_barrier
	ds_read_b128 v[8:11], v0
	ds_read_b128 v[0:3], v0 offset:2048
	ds_read_b128 v[12:15], v4
	ds_read_b128 v[4:7], v4 offset:2048
	ds_read_b128 v[56:59], v200 offset:32768
	ds_read_b128 v[48:51], v200 offset:34816
	ds_read_b128 v[60:63], v201 offset:32768
	ds_read_b128 v[52:55], v201 offset:34816
	ds_read_b128 v[40:43], v200 offset:36864
	ds_read_b128 v[32:35], v200 offset:38912
	ds_read_b128 v[44:47], v201 offset:36864
	ds_read_b128 v[36:39], v201 offset:38912
	s_waitcnt vmcnt(8)
	s_and_b64 vcc, exec, s[0:1]
	s_cbranch_vccnz .LBB4_24
	s_add_u32 s52, s49, 0x40100
	s_addc_u32 s13, s50, 0
	s_and_b32 s53, s13, 0xffff
	s_mov_b32 s54, s14
	s_mov_b32 s55, s15
	s_mov_b32 m0, s34
	s_nop 0
	buffer_load_dwordx4 v192, s[52:55], 0 offen lds
	s_mov_b32 m0, s35
	s_nop 0
	buffer_load_dwordx4 v194, s[52:55], 0 offen lds
.LBB4_24:
	s_waitcnt lgkmcnt(8)
	s_barrier
	s_waitcnt lgkmcnt(0)
	s_setprio 0
	v_mfma_f32_16x16x128_f8f6f4 v[188:191], v[8:15], v[56:63], v[188:191]
	v_mfma_f32_16x16x128_f8f6f4 v[184:187], v[0:7], v[56:63], v[184:187]
	v_mfma_f32_16x16x128_f8f6f4 v[172:175], v[8:15], v[48:55], v[172:175]
	v_mfma_f32_16x16x128_f8f6f4 v[168:171], v[0:7], v[48:55], v[168:171]
	v_mfma_f32_16x16x128_f8f6f4 v[156:159], v[8:15], v[40:47], v[156:159]
	v_mfma_f32_16x16x128_f8f6f4 v[152:155], v[0:7], v[40:47], v[152:155]
	v_mfma_f32_16x16x128_f8f6f4 v[140:143], v[8:15], v[32:39], v[140:143]
	v_mfma_f32_16x16x128_f8f6f4 v[136:139], v[0:7], v[32:39], v[136:139]
	s_setprio 1
	s_barrier
	s_add_i32 s13, 0, 0x1c000
	v_add_u32_e32 v16, s13, v198
	v_add_u32_e32 v20, s13, v199
	ds_read_b128 v[24:27], v16
	ds_read_b128 v[16:19], v16 offset:2048
	ds_read_b128 v[28:31], v20
	ds_read_b128 v[20:23], v20 offset:2048
	s_waitcnt vmcnt(8)
	s_and_b64 vcc, exec, s[0:1]
	s_cbranch_vccnz .LBB4_26
	s_and_b64 s[22:23], exec, s[18:19]
	s_cselect_b32 s20, s8, s20
	s_cselect_b32 s13, s3, s48
	s_add_u32 s48, s20, 0x80
	s_addc_u32 s13, s13, 0
	s_and_b32 s49, s13, 0xffff
	s_mov_b32 s50, s14
	s_mov_b32 s51, s15
	s_mov_b32 m0, s36
	s_nop 0
	buffer_load_dwordx4 v193, s[48:51], 0 offen lds
	s_mov_b32 m0, s37
	s_nop 0
	buffer_load_dwordx4 v195, s[48:51], 0 offen lds
.LBB4_26:
	s_barrier
	s_waitcnt lgkmcnt(0)
	s_setprio 0
	v_mfma_f32_16x16x128_f8f6f4 v[180:183], v[24:31], v[56:63], v[180:183]
	v_mfma_f32_16x16x128_f8f6f4 v[176:179], v[16:23], v[56:63], v[176:179]
	v_mfma_f32_16x16x128_f8f6f4 v[164:167], v[24:31], v[48:55], v[164:167]
	v_mfma_f32_16x16x128_f8f6f4 v[160:163], v[16:23], v[48:55], v[160:163]
	v_mfma_f32_16x16x128_f8f6f4 v[148:151], v[24:31], v[40:47], v[148:151]
	v_mfma_f32_16x16x128_f8f6f4 v[144:147], v[16:23], v[40:47], v[144:147]
	v_mfma_f32_16x16x128_f8f6f4 v[132:135], v[24:31], v[32:39], v[132:135]
	v_mfma_f32_16x16x128_f8f6f4 v[128:131], v[16:23], v[32:39], v[128:131]
	s_setprio 1
	s_barrier
	ds_read_b128 v[56:59], v200 offset:49152
	ds_read_b128 v[48:51], v200 offset:51200
	ds_read_b128 v[60:63], v201 offset:49152
	ds_read_b128 v[52:55], v201 offset:51200
	ds_read_b128 v[40:43], v200 offset:53248
	ds_read_b128 v[32:35], v200 offset:55296
	ds_read_b128 v[44:47], v201 offset:53248
	ds_read_b128 v[36:39], v201 offset:55296
	s_and_b64 vcc, exec, s[0:1]
	s_cbranch_vccnz .LBB4_28
	s_and_b64 s[18:19], exec, s[18:19]
	s_cselect_b32 s12, s16, s12
	s_cselect_b32 s13, s9, s21
	s_add_u32 s12, s12, 0x80
	s_addc_u32 s13, s13, 0
	s_and_b32 s13, s13, 0xffff
	s_mov_b32 m0, s38
	s_nop 0
	buffer_load_dwordx4 v192, s[12:15], 0 offen lds
	s_mov_b32 m0, s39
	s_nop 0
	buffer_load_dwordx4 v194, s[12:15], 0 offen lds
.LBB4_28:
	s_barrier
	s_waitcnt lgkmcnt(0)
	s_setprio 0
	v_mfma_f32_16x16x128_f8f6f4 v[124:127], v[8:15], v[56:63], v[124:127]
	v_mfma_f32_16x16x128_f8f6f4 v[120:123], v[0:7], v[56:63], v[120:123]
	v_mfma_f32_16x16x128_f8f6f4 v[108:111], v[8:15], v[48:55], v[108:111]
	v_mfma_f32_16x16x128_f8f6f4 v[104:107], v[0:7], v[48:55], v[104:107]
	v_mfma_f32_16x16x128_f8f6f4 v[92:95], v[8:15], v[40:47], v[92:95]
	v_mfma_f32_16x16x128_f8f6f4 v[88:91], v[0:7], v[40:47], v[88:91]
	v_mfma_f32_16x16x128_f8f6f4 v[76:79], v[8:15], v[32:39], v[76:79]
	v_mfma_f32_16x16x128_f8f6f4 v[72:75], v[0:7], v[32:39], v[72:75]
	s_setprio 1
	s_barrier
	s_and_b64 vcc, exec, s[0:1]
	s_cbranch_vccnz .LBB4_13
	s_add_u32 s12, s46, 0x4180
	s_addc_u32 s0, s47, 0
	s_and_b32 s13, s0, 0xffff
	s_mov_b32 m0, s40
	s_nop 0
	buffer_load_dwordx4 v193, s[12:15], 0 offen lds
	s_mov_b32 m0, s41
	s_nop 0
	buffer_load_dwordx4 v195, s[12:15], 0 offen lds
	s_branch .LBB4_13

.LBB5_17:
	s_waitcnt vmcnt(10)
	s_barrier
	s_setprio 0
	v_mfma_f32_16x16x128_f8f6f4 v[108:111], v[24:31], v[56:63], v[108:111]
	s_add_i32 s45, s45, 2
	s_add_u32 s14, s14, 0x100
	s_addc_u32 s15, s15, 0
	v_mfma_f32_16x16x128_f8f6f4 v[104:107], v[16:23], v[56:63], v[104:107]
	s_cmpk_eq_i32 s14, 0x700
	s_cselect_b64 s[18:19], -1, 0
	s_cmpk_lg_i32 s14, 0x700
	s_cselect_b64 s[26:27], -1, 0
	v_mfma_f32_16x16x128_f8f6f4 v[92:95], v[24:31], v[48:55], v[92:95]
	s_add_u32 s50, s16, s14
	s_addc_u32 s51, s13, s15
	s_add_u32 s47, s12, s14
	s_addc_u32 s48, s7, s15
	v_mfma_f32_16x16x128_f8f6f4 v[88:91], v[16:23], v[48:55], v[88:91]
	s_add_u32 s20, s47, 0x100
	s_addc_u32 s49, s48, 0
	s_add_u32 s8, s50, 0x40080
	s_addc_u32 s0, s51, 0
	v_mfma_f32_16x16x128_f8f6f4 v[80:83], v[24:31], v[40:47], v[80:83]
	s_and_b32 s9, s0, 0xffff
	s_cmp_gt_u32 s45, 13
	v_mfma_f32_16x16x128_f8f6f4 v[76:79], v[16:23], v[40:47], v[76:79]
	v_mfma_f32_16x16x128_f8f6f4 v[68:71], v[24:31], v[32:39], v[68:71]
	v_mfma_f32_16x16x128_f8f6f4 v[64:67], v[16:23], v[32:39], v[64:67]
	s_setprio 1
	s_barrier
	s_cbranch_scc1 .LBB5_34
.LBB5_18:
	ds_read_b128 v[0:3], v200
	ds_read_b128 v[8:11], v200 offset:2048
	ds_read_b128 v[4:7], v201
	ds_read_b128 v[12:15], v201 offset:2048
	s_mov_b32 m0, s43
	ds_read_b128 v[56:59], v198
	ds_read_b128 v[48:51], v198 offset:2048
	ds_read_b128 v[60:63], v199
	ds_read_b128 v[52:55], v199 offset:2048
	ds_read_b128 v[40:43], v198 offset:4096
	ds_read_b128 v[32:35], v198 offset:6144
	ds_read_b128 v[44:47], v199 offset:4096
	ds_read_b128 v[36:39], v199 offset:6144
	s_waitcnt vmcnt(8)
	buffer_load_dwordx4 v192, s[8:11], 0 offen lds
	s_mov_b32 m0, s44
	s_nop 0
	buffer_load_dwordx4 v193, s[8:11], 0 offen lds
	s_waitcnt lgkmcnt(8)
	s_barrier
	s_waitcnt lgkmcnt(0)
	s_setprio 0
	v_mfma_f32_16x16x128_f8f6f4 v[188:191], v[0:7], v[56:63], v[188:191]
	v_mfma_f32_16x16x128_f8f6f4 v[184:187], v[8:15], v[56:63], v[184:187]
	v_mfma_f32_16x16x128_f8f6f4 v[176:179], v[0:7], v[48:55], v[176:179]
	v_mfma_f32_16x16x128_f8f6f4 v[168:171], v[8:15], v[48:55], v[168:171]
	v_mfma_f32_16x16x128_f8f6f4 v[160:163], v[0:7], v[40:47], v[160:163]
	v_mfma_f32_16x16x128_f8f6f4 v[152:155], v[8:15], v[40:47], v[152:155]
	v_mfma_f32_16x16x128_f8f6f4 v[144:147], v[0:7], v[32:39], v[144:147]
	v_mfma_f32_16x16x128_f8f6f4 v[136:139], v[8:15], v[32:39], v[136:139]
	s_setprio 1
	s_barrier
	ds_read_b128 v[24:27], v202
	ds_read_b128 v[16:19], v202 offset:2048
	ds_read_b128 v[28:31], v203
	ds_read_b128 v[20:23], v203 offset:2048
	s_waitcnt vmcnt(8)
	s_and_b64 vcc, exec, s[18:19]
	s_cbranch_vccnz .LBB5_20
	s_and_b32 s21, s49, 0xffff
	s_mov_b32 s22, s10
	s_mov_b32 s23, s11
	s_mov_b32 m0, s29
	s_nop 0
	buffer_load_dwordx4 v192, s[20:23], 0 offen lds
	s_mov_b32 m0, s30
	s_nop 0
	buffer_load_dwordx4 v193, s[20:23], 0 offen lds
.LBB5_20:
	s_barrier
	s_waitcnt lgkmcnt(0)
	s_setprio 0
	v_mfma_f32_16x16x128_f8f6f4 v[180:183], v[24:31], v[56:63], v[180:183]
	s_add_u32 s8, s50, 0x100
	s_addc_u32 s21, s51, 0
	v_mfma_f32_16x16x128_f8f6f4 v[172:175], v[16:23], v[56:63], v[172:175]
	v_mfma_f32_16x16x128_f8f6f4 v[164:167], v[24:31], v[48:55], v[164:167]
	v_mfma_f32_16x16x128_f8f6f4 v[156:159], v[16:23], v[48:55], v[156:159]
	v_mfma_f32_16x16x128_f8f6f4 v[148:151], v[24:31], v[40:47], v[148:151]
	v_mfma_f32_16x16x128_f8f6f4 v[140:143], v[16:23], v[40:47], v[140:143]
	v_mfma_f32_16x16x128_f8f6f4 v[132:135], v[24:31], v[32:39], v[132:135]
	v_mfma_f32_16x16x128_f8f6f4 v[128:131], v[16:23], v[32:39], v[128:131]
	s_setprio 1
	s_barrier
	ds_read_b128 v[56:59], v198 offset:16384
	ds_read_b128 v[48:51], v198 offset:18432
	ds_read_b128 v[60:63], v199 offset:16384
	ds_read_b128 v[52:55], v199 offset:18432
	ds_read_b128 v[40:43], v198 offset:20480
	ds_read_b128 v[32:35], v198 offset:22528
	ds_read_b128 v[44:47], v199 offset:20480
	ds_read_b128 v[36:39], v199 offset:22528
	v_cndmask_b32_e64 v204, 0, 1, s[26:27]
	v_cmp_ne_u32_e64 s[0:1], 1, v204
	s_andn2_b64 vcc, exec, s[26:27]
	s_cbranch_vccnz .LBB5_22
	s_and_b32 s9, s21, 0xffff
	s_mov_b32 m0, s25
	s_nop 0
	buffer_load_dwordx4 v192, s[8:11], 0 offen lds
	s_mov_b32 m0, s31
	s_nop 0
	buffer_load_dwordx4 v193, s[8:11], 0 offen lds
.LBB5_22:
	s_barrier
	s_waitcnt lgkmcnt(0)
	s_setprio 0
	v_mfma_f32_16x16x128_f8f6f4 v[124:127], v[0:7], v[56:63], v[124:127]
	v_mfma_f32_16x16x128_f8f6f4 v[120:123], v[8:15], v[56:63], v[120:123]
	v_mfma_f32_16x16x128_f8f6f4 v[116:119], v[0:7], v[48:55], v[116:119]
	v_mfma_f32_16x16x128_f8f6f4 v[112:115], v[8:15], v[48:55], v[112:115]
	v_mfma_f32_16x16x128_f8f6f4 v[100:103], v[0:7], v[40:47], v[100:103]
	v_mfma_f32_16x16x128_f8f6f4 v[96:99], v[8:15], v[40:47], v[96:99]
	v_mfma_f32_16x16x128_f8f6f4 v[84:87], v[0:7], v[32:39], v[84:87]
	v_mfma_f32_16x16x128_f8f6f4 v[72:75], v[8:15], v[32:39], v[72:75]
	s_setprio 1
	s_barrier
	s_and_b64 vcc, exec, s[0:1]
	s_mov_b64 s[22:23], -1
	s_cbranch_vccnz .LBB5_24
	s_add_u32 s52, s47, 0x40100
	s_addc_u32 s9, s48, 0
	s_mov_b32 m0, s17
	s_and_b32 s53, s9, 0xffff
	s_mov_b32 s54, s10
	s_mov_b32 s55, s11
	buffer_load_dwordx4 v192, s[52:55], 0 offen lds
	s_mov_b32 m0, s33
	s_mov_b64 s[22:23], 0
	buffer_load_dwordx4 v193, s[52:55], 0 offen lds
	s_waitcnt vmcnt(10)

.LBB5_26:
	s_barrier
	s_setprio 0
	v_mfma_f32_16x16x128_f8f6f4 v[108:111], v[24:31], v[56:63], v[108:111]
	v_add_u32_e32 v0, s46, v196
	v_add_u32_e32 v4, s46, v197
	v_mfma_f32_16x16x128_f8f6f4 v[104:107], v[16:23], v[56:63], v[104:107]
	v_mfma_f32_16x16x128_f8f6f4 v[92:95], v[24:31], v[48:55], v[92:95]
	v_mfma_f32_16x16x128_f8f6f4 v[88:91], v[16:23], v[48:55], v[88:91]
	v_mfma_f32_16x16x128_f8f6f4 v[80:83], v[24:31], v[40:47], v[80:83]
	v_mfma_f32_16x16x128_f8f6f4 v[76:79], v[16:23], v[40:47], v[76:79]
	v_mfma_f32_16x16x128_f8f6f4 v[68:71], v[24:31], v[32:39], v[68:71]
	v_mfma_f32_16x16x128_f8f6f4 v[64:67], v[16:23], v[32:39], v[64:67]
	s_setprio 1
	s_barrier
	ds_read_b128 v[8:11], v0
	ds_read_b128 v[0:3], v0 offset:2048
	ds_read_b128 v[12:15], v4
	ds_read_b128 v[4:7], v4 offset:2048
	ds_read_b128 v[56:59], v198 offset:32768
	ds_read_b128 v[48:51], v198 offset:34816
	ds_read_b128 v[60:63], v199 offset:32768
	ds_read_b128 v[52:55], v199 offset:34816
	ds_read_b128 v[40:43], v198 offset:36864
	ds_read_b128 v[32:35], v198 offset:38912
	ds_read_b128 v[44:47], v199 offset:36864
	ds_read_b128 v[36:39], v199 offset:38912
	s_waitcnt vmcnt(8)
	s_and_b64 vcc, exec, s[0:1]
	s_cbranch_vccnz .LBB5_28
	s_add_u32 s52, s50, 0x40100
	s_addc_u32 s9, s51, 0
	s_and_b32 s53, s9, 0xffff
	s_mov_b32 s54, s10
	s_mov_b32 s55, s11
	s_mov_b32 m0, s34
	s_nop 0
	buffer_load_dwordx4 v192, s[52:55], 0 offen lds
	s_mov_b32 m0, s36
	s_nop 0
	buffer_load_dwordx4 v193, s[52:55], 0 offen lds
.LBB5_28:
	s_waitcnt lgkmcnt(8)
	s_barrier
	s_waitcnt lgkmcnt(0)
	s_setprio 0
	v_mfma_f32_16x16x128_f8f6f4 v[188:191], v[8:15], v[56:63], v[188:191]
	v_mfma_f32_16x16x128_f8f6f4 v[184:187], v[0:7], v[56:63], v[184:187]
	v_mfma_f32_16x16x128_f8f6f4 v[176:179], v[8:15], v[48:55], v[176:179]
	v_mfma_f32_16x16x128_f8f6f4 v[168:171], v[0:7], v[48:55], v[168:171]
	v_mfma_f32_16x16x128_f8f6f4 v[160:163], v[8:15], v[40:47], v[160:163]
	v_mfma_f32_16x16x128_f8f6f4 v[152:155], v[0:7], v[40:47], v[152:155]
	v_mfma_f32_16x16x128_f8f6f4 v[144:147], v[8:15], v[32:39], v[144:147]
	v_mfma_f32_16x16x128_f8f6f4 v[136:139], v[0:7], v[32:39], v[136:139]
	s_setprio 1
	s_barrier
	s_add_i32 s9, 0, 0x1c000
	v_add_u32_e32 v16, s9, v196
	v_add_u32_e32 v20, s9, v197
	ds_read_b128 v[24:27], v16
	ds_read_b128 v[16:19], v16 offset:2048
	ds_read_b128 v[28:31], v20
	ds_read_b128 v[20:23], v20 offset:2048
	s_waitcnt vmcnt(8)
	s_and_b64 vcc, exec, s[0:1]
	s_cbranch_vccnz .LBB5_30
	s_and_b64 s[22:23], exec, s[18:19]
	s_cselect_b32 s20, s12, s20
	s_cselect_b32 s9, s7, s49
	s_add_u32 s52, s20, 0x80
	s_addc_u32 s9, s9, 0
	s_and_b32 s53, s9, 0xffff
	s_mov_b32 s54, s10
	s_mov_b32 s55, s11
	s_mov_b32 m0, s37
	s_nop 0
	buffer_load_dwordx4 v192, s[52:55], 0 offen lds
	s_mov_b32 m0, s38
	s_nop 0
	buffer_load_dwordx4 v193, s[52:55], 0 offen lds
.LBB5_30:
	s_barrier
	s_waitcnt lgkmcnt(0)
	s_setprio 0
	v_mfma_f32_16x16x128_f8f6f4 v[180:183], v[24:31], v[56:63], v[180:183]
	v_mfma_f32_16x16x128_f8f6f4 v[172:175], v[16:23], v[56:63], v[172:175]
	v_mfma_f32_16x16x128_f8f6f4 v[164:167], v[24:31], v[48:55], v[164:167]
	v_mfma_f32_16x16x128_f8f6f4 v[156:159], v[16:23], v[48:55], v[156:159]
	v_mfma_f32_16x16x128_f8f6f4 v[148:151], v[24:31], v[40:47], v[148:151]
	v_mfma_f32_16x16x128_f8f6f4 v[140:143], v[16:23], v[40:47], v[140:143]
	v_mfma_f32_16x16x128_f8f6f4 v[132:135], v[24:31], v[32:39], v[132:135]
	v_mfma_f32_16x16x128_f8f6f4 v[128:131], v[16:23], v[32:39], v[128:131]
	s_setprio 1
	s_barrier
	ds_read_b128 v[56:59], v198 offset:49152
	ds_read_b128 v[48:51], v198 offset:51200
	ds_read_b128 v[60:63], v199 offset:49152
	ds_read_b128 v[52:55], v199 offset:51200
	ds_read_b128 v[40:43], v198 offset:53248
	ds_read_b128 v[32:35], v198 offset:55296
	ds_read_b128 v[44:47], v199 offset:53248
	ds_read_b128 v[36:39], v199 offset:55296
	s_and_b64 vcc, exec, s[0:1]
	s_cbranch_vccnz .LBB5_32
	s_and_b64 s[18:19], exec, s[18:19]
	s_cselect_b32 s8, s16, s8
	s_cselect_b32 s9, s13, s21
	s_add_u32 s8, s8, 0x80
	s_addc_u32 s9, s9, 0
	s_and_b32 s9, s9, 0xffff
	s_mov_b32 m0, s39
	s_nop 0
	buffer_load_dwordx4 v192, s[8:11], 0 offen lds
	s_mov_b32 m0, s40
	s_nop 0
	buffer_load_dwordx4 v193, s[8:11], 0 offen lds
.LBB5_32:
	s_barrier
	s_waitcnt lgkmcnt(0)
	s_setprio 0
	v_mfma_f32_16x16x128_f8f6f4 v[124:127], v[8:15], v[56:63], v[124:127]
	v_mfma_f32_16x16x128_f8f6f4 v[120:123], v[0:7], v[56:63], v[120:123]
	v_mfma_f32_16x16x128_f8f6f4 v[116:119], v[8:15], v[48:55], v[116:119]
	v_mfma_f32_16x16x128_f8f6f4 v[112:115], v[0:7], v[48:55], v[112:115]
	v_mfma_f32_16x16x128_f8f6f4 v[100:103], v[8:15], v[40:47], v[100:103]
	v_mfma_f32_16x16x128_f8f6f4 v[96:99], v[0:7], v[40:47], v[96:99]
	v_mfma_f32_16x16x128_f8f6f4 v[84:87], v[8:15], v[32:39], v[84:87]
	v_mfma_f32_16x16x128_f8f6f4 v[72:75], v[0:7], v[32:39], v[72:75]
	s_setprio 1
	s_barrier
	s_and_b64 vcc, exec, s[0:1]
	s_cbranch_vccnz .LBB5_17
	s_add_u32 s8, s47, 0x40180
	s_addc_u32 s0, s48, 0
	s_and_b32 s9, s0, 0xffff
	s_mov_b32 m0, s41
	s_nop 0
	buffer_load_dwordx4 v192, s[8:11], 0 offen lds
	s_mov_b32 m0, s42
	s_nop 0
	buffer_load_dwordx4 v193, s[8:11], 0 offen lds
	s_branch .LBB5_17
